# baseline (speedup 1.0000x reference)
.LBB1_6:
	s_cmp_eq_u32 s15, 3
	s_cselect_b32 s46, 1, 0
	s_cmp_eq_u32 s14, 3
	s_cbranch_scc0 .Lsib_nolag
	s_sleep 10
.Lsib_nolag:
	s_and_b32 s16, s2, 7
	s_mul_i32 s0, s16, 0x4b
	s_add_i32 s22, s3, s0
	s_lshr_b32 s23, s25, 6
	s_cmp_ge_u32 s23, s14
	s_cselect_b64 s[0:1], -1, 0
	s_cmp_lt_u32 s23, s15
	s_cselect_b64 s[2:3], -1, 0
	s_and_b64 s[8:9], s[0:1], s[2:3]
	s_mul_i32 s2, s22, 0x28000
	s_movk_i32 s0, 0xc0
	s_mul_hi_u32 s1, s22, 0x28000
	s_waitcnt lgkmcnt(0)
	s_add_u32 s2, s4, s2
	v_lshlrev_b32_e32 v1, 2, v0
	s_addc_u32 s3, s5, s1
	v_add_u32_e32 v2, 0x500, v1
	v_cmp_gt_u32_e64 s[0:1], s0, v0
	v_lshlrev_b32_e32 v104, 4, v0
	s_mul_i32 s16, s16, 5
	v_cndmask_b32_e64 v1, v1, v2, s[0:1]
	v_lshlrev_b32_e32 v2, 2, v1
	s_cmp_eq_u32 s46, 0
	s_cbranch_scc1 .Lnq0
	global_load_dwordx4 v[68:71], v104, s[2:3]
	s_and_saveexec_b64 s[44:45], s[0:1]
	global_load_dwordx4 v[64:67], v2, s[2:3]
	s_branch .Ldq0
.Lnq0:
	global_load_dwordx4 v[68:71], v104, s[2:3] nt
	s_and_saveexec_b64 s[44:45], s[0:1]
	global_load_dwordx4 v[64:67], v2, s[2:3] nt
.Ldq0:
	s_mov_b64 exec, s[44:45]
	s_add_i32 s24, s23, s16
	v_mov_b32_e32 v105, 0
	s_mul_i32 s4, s24, 20
	s_mov_b32 s5, 0
	v_mov_b32_e32 v3, v105
	v_lshrrev_b32_e32 v1, 4, v0
	s_lshl_b64 s[14:15], s[4:5], 12
	v_lshlrev_b32_e32 v6, 3, v0
	v_lshl_add_u64 v[96:97], s[2:3], 0, v[104:105]
	v_lshl_add_u64 v[98:99], s[2:3], 0, v[2:3]
	s_add_u32 s2, s6, s14
	v_and_b32_e32 v104, 0x3f0, v104
	s_addc_u32 s3, s7, s15
	v_lshl_add_u64 v[2:3], s[2:3], 0, v[104:105]
	s_mov_b64 s[14:15], 0x32000
	s_mov_b32 s4, 0x32000
	v_lshl_add_u64 v[100:101], v[2:3], 0, s[14:15]
	v_add_co_u32_e32 v2, vcc, s4, v2
	s_nop 1
	v_addc_co_u32_e32 v3, vcc, 0, v3, vcc
	s_and_saveexec_b64 s[44:45], s[8:9]
	global_load_dwordx4 v[80:83], v[100:101], off offset:1024
	global_load_dwordx4 v[88:91], v[100:101], off offset:2048
	global_load_dwordx4 v[92:95], v[2:3], off
	global_load_dwordx4 v[84:87], v[100:101], off offset:3072
	s_mov_b64 exec, s[44:45]
	s_movk_i32 s4, 0x2000
	v_add_co_u32_e32 v2, vcc, s4, v96
	s_nop 1
	v_addc_co_u32_e32 v3, vcc, 0, v97, vcc
	v_add_co_u32_e32 v4, vcc, s4, v98
	s_nop 1
	v_addc_co_u32_e32 v5, vcc, 0, v99, vcc
	s_cmp_eq_u32 s46, 0
	s_cbranch_scc1 .Lnq1
	global_load_dwordx4 v[76:79], v[2:3], off
	s_and_saveexec_b64 s[44:45], s[0:1]
	global_load_dwordx4 v[72:75], v[4:5], off
	s_branch .Ldq1
.Lnq1:
	global_load_dwordx4 v[76:79], v[2:3], off nt
	s_and_saveexec_b64 s[44:45], s[0:1]
	global_load_dwordx4 v[72:75], v[4:5], off nt
.Ldq1:
	s_mov_b64 exec, s[44:45]
	v_bfe_u32 v2, v0, 2, 4
	v_and_b32_e32 v0, 63, v0
	v_mul_u32_u24_e32 v2, 0xa0, v2
	v_lshlrev_b32_e32 v104, 4, v0
	v_and_or_b32 v108, v6, 24, v2
	v_mul_u32_u24_e32 v2, 0xa0, v1
	v_and_b32_e32 v3, 0x78, v6
	v_lshl_add_u64 v[0:1], s[2:3], 0, v[104:105]
	s_mov_b64 s[2:3], 0x33c00
	v_mov_b32_e32 v60, v105
	v_mov_b32_e32 v61, v105
	v_lshl_add_u64 v[102:103], v[0:1], 0, s[2:3]
	v_mov_b32_e32 v104, v105
	v_mov_b32_e32 v62, v105
	v_mov_b32_e32 v63, v105
	v_add_u32_e32 v109, v2, v3
	v_mov_b64_e32 v[56:57], v[60:61]
	v_mov_b64_e32 v[52:53], v[60:61]
	v_mov_b64_e32 v[48:49], v[60:61]
	v_mov_b64_e32 v[44:45], v[60:61]
	v_mov_b64_e32 v[40:41], v[60:61]
	v_mov_b64_e32 v[36:37], v[60:61]
	v_mov_b64_e32 v[32:33], v[60:61]
	v_mov_b64_e32 v[28:29], v[60:61]
	v_mov_b64_e32 v[24:25], v[60:61]
	v_mov_b64_e32 v[20:21], v[60:61]
	v_mov_b64_e32 v[16:17], v[60:61]
	v_mov_b64_e32 v[12:13], v[60:61]
	v_mov_b64_e32 v[8:9], v[60:61]
	v_mov_b64_e32 v[4:5], v[60:61]
	v_mov_b64_e32 v[0:1], v[60:61]
	s_mov_b64 s[14:15], 0x2000
	v_mov_b64_e32 v[58:59], v[62:63]
	v_mov_b64_e32 v[54:55], v[62:63]
	v_mov_b64_e32 v[50:51], v[62:63]
	v_mov_b64_e32 v[46:47], v[62:63]
	v_mov_b64_e32 v[42:43], v[62:63]
	v_mov_b64_e32 v[38:39], v[62:63]
	v_mov_b64_e32 v[34:35], v[62:63]
	v_mov_b64_e32 v[30:31], v[62:63]
	v_mov_b64_e32 v[26:27], v[62:63]
	v_mov_b64_e32 v[22:23], v[62:63]
	v_mov_b64_e32 v[18:19], v[62:63]
	v_mov_b64_e32 v[14:15], v[62:63]
	v_mov_b64_e32 v[10:11], v[62:63]
	v_mov_b64_e32 v[6:7], v[62:63]
	v_mov_b64_e32 v[2:3], v[62:63]
	s_mov_b32 s26, 0
	v_mov_b64_e32 v[106:107], v[104:105]

.LBB1_18:
	s_and_saveexec_b64 s[44:45], s[8:9]
	global_load_dwordx4 v[84:87], v[102:103], off offset:-3072
	global_load_dwordx4 v[88:91], v[102:103], off offset:-2048
	global_load_dwordx4 v[92:95], v[102:103], off offset:-1024
	global_load_dwordx4 v[80:83], v[102:103], off
	s_mov_b64 exec, s[44:45]
	s_add_i32 s27, s26, 2
	s_cmp_gt_u32 s26, 17
	s_cselect_b64 s[16:17], -1, 0
	s_cmp_lt_u32 s26, 18
	s_cselect_b64 s[18:19], -1, 0
	s_and_b64 s[20:21], s[18:19], exec
	s_cselect_b32 s4, s27, s26
	s_lshl_b32 s4, s4, 11
	s_lshl_b64 s[20:21], s[4:5], 2
	v_lshl_add_u64 v[64:65], v[96:97], 0, s[20:21]
	v_lshl_add_u64 v[66:67], v[98:99], 0, s[20:21]
	s_and_saveexec_b64 s[44:45], s[18:19]
	s_cmp_eq_u32 s46, 0
	s_cbranch_scc1 .Lnq2
	global_load_dwordx4 v[68:71], v[64:65], off
	s_and_b64 exec, exec, s[0:1]
	global_load_dwordx4 v[64:67], v[66:67], off
	s_branch .Ldq2
.Lnq2:
	global_load_dwordx4 v[68:71], v[64:65], off nt
	s_and_b64 exec, exec, s[0:1]
	global_load_dwordx4 v[64:67], v[66:67], off nt
.Ldq2:
	s_mov_b64 exec, s[44:45]
	s_waitcnt vmcnt(7)
	v_pk_fma_f32 v[104:105], v[76:77], v[76:77], v[104:105]
	v_pk_fma_f32 v[106:107], v[78:79], v[78:79], v[106:107]
	v_cvt_pk_f16_f32 v79, v78, v79
	v_cvt_pk_f16_f32 v78, v76, v77
	ds_write_b64 v109, v[78:79] offset:5120
	s_and_saveexec_b64 s[20:21], s[0:1]
	s_cbranch_execz .LBB1_20
	s_waitcnt vmcnt(6)
	v_pk_fma_f32 v[104:105], v[72:73], v[72:73], v[104:105]
	v_pk_fma_f32 v[106:107], v[74:75], v[74:75], v[106:107]
	v_cvt_pk_f16_f32 v75, v74, v75
	v_cvt_pk_f16_f32 v74, v72, v73
	ds_write_b64 v109, v[74:75] offset:8320

.LBB1_29:
	s_add_i32 s20, s26, 1
	s_and_b64 s[2:3], s[18:19], exec
	s_cselect_b32 s2, s27, s20
	s_lshl_b32 s4, s2, 12
	s_waitcnt vmcnt(6)
	v_lshl_add_u64 v[72:73], v[100:101], 0, s[4:5]
	s_and_saveexec_b64 s[44:45], s[8:9]
	s_and_b64 exec, exec, s[18:19]
	global_load_dwordx4 v[92:95], v[72:73], off
	global_load_dwordx4 v[80:83], v[72:73], off offset:1024
	global_load_dwordx4 v[88:91], v[72:73], off offset:2048
	global_load_dwordx4 v[84:87], v[72:73], off offset:3072
	s_mov_b64 exec, s[44:45]
	s_add_i32 s2, s26, 3
	s_cmp_lt_u32 s26, 17
	s_cselect_b32 s2, s2, s20
	s_lshl_b32 s4, s2, 11
	s_lshl_b64 s[2:3], s[4:5], 2
	v_lshl_add_u64 v[72:73], v[96:97], 0, s[2:3]
	v_lshl_add_u64 v[74:75], v[98:99], 0, s[2:3]
	s_and_saveexec_b64 s[44:45], s[18:19]
	s_cmp_eq_u32 s46, 0
	s_cbranch_scc1 .Lnq3
	global_load_dwordx4 v[76:79], v[72:73], off
	s_and_b64 exec, exec, s[0:1]
	global_load_dwordx4 v[72:75], v[74:75], off
	s_branch .Ldq3
.Lnq3:
	global_load_dwordx4 v[76:79], v[72:73], off nt
	s_and_b64 exec, exec, s[0:1]
	global_load_dwordx4 v[72:75], v[74:75], off nt
.Ldq3:
	s_mov_b64 exec, s[44:45]
	v_lshl_add_u64 v[102:103], v[102:103], 0, s[14:15]
	s_and_b64 vcc, exec, s[16:17]
	s_cbranch_vccnz .LBB1_31
	s_mov_b32 s26, s27
	s_branch .LBB1_7
